# speedup vs baseline: 1.0656x; 1.0099x over previous
_Z11gat2_kernelPKfPKDF16_S0_S2_S0_PDF16_PfS2_S2_S0_S4_:
	s_cmp_lt_u32 s2, 8
	s_cbranch_scc1 .Lg2attn
	s_load_dwordx4 s[4:7], s[0:1], 0x10
	v_and_b32_e32 v1, 63, v0
	v_lshrrev_b32_e32 v197, 6, v0
	v_and_b32_e32 v198, 31, v0
	v_bfe_u32 v199, v0, 5, 1
	s_mov_b64 s[8:9], -1
	s_cmp_lt_u32 s2, 8
	v_lshlrev_b32_e32 v202, 8, v0
	v_lshlrev_b32_e32 v201, 3, v1
	v_lshlrev_b32_e32 v200, 4, v1
	v_mbcnt_lo_u32_b32 v196, -1, 0
	s_cbranch_scc0 .LBB3_8

.Lg2attn:
	s_load_dwordx8 s[4:11], s[0:1], 0x0
	s_load_dwordx4 s[12:15], s[0:1], 0x20
	s_load_dwordx2 s[16:17], s[0:1], 0x30
	v_and_b32_e32 v1, 63, v0
	v_and_b32_e32 v2, 31, v0
	v_lshrrev_b32_e32 v5, 6, v0
	v_and_b32_e32 v3, 32, v0
	v_lshlrev_b32_e32 v4, 4, v1
	v_readfirstlane_b32 s19, v5
	s_lshl_b32 s18, s2, 5
	v_lshlrev_b32_e32 v12, 2, v0
	v_add_u32_e32 v13, s18, v2
	v_lshlrev_b32_e32 v13, 2, v13
	v_lshl_add_u32 v17, v5, 6, v2
	v_lshlrev_b32_e32 v17, 2, v17
	v_add_u32_e32 v14, 0x1000, v4
	v_add_u32_e32 v15, 0x2000, v4
	v_add_u32_e32 v16, 0x3000, v4
	s_lshl_b32 s26, s19, 15
	s_lshl_b32 s27, s19, 14
	s_waitcnt lgkmcnt(0)
	s_add_u32 s20, s6, s26
	s_addc_u32 s21, s7, 0
	s_add_u32 s22, s20, 0x4000
	s_addc_u32 s23, s21, 0
	s_add_u32 s24, s10, s27
	s_addc_u32 s25, s11, 0
	global_load_dwordx4 v[28:31], v4, s[4:5]
	global_load_dword v6, v12, s[4:5]
	global_load_dword v7, v13, s[4:5] offset:1024
	global_load_dword v8, v12, s[12:13]
	global_load_dword v9, v12, s[12:13] offset:1024
	global_load_dword v10, v17, s[8:9]
	global_load_dword v11, v17, s[8:9] offset:128
	global_load_dwordx4 a[0:3], v4, s[20:21]
	global_load_dwordx4 a[4:7], v4, s[22:23]
	global_load_dwordx4 a[8:11], v4, s[20:21] offset:1024
	global_load_dwordx4 a[12:15], v4, s[22:23] offset:1024
	global_load_dwordx4 a[16:19], v4, s[20:21] offset:2048
	global_load_dwordx4 a[20:23], v4, s[22:23] offset:2048
	global_load_dwordx4 a[24:27], v4, s[20:21] offset:3072
	global_load_dwordx4 a[28:31], v4, s[22:23] offset:3072
	global_load_dwordx4 a[32:35], v14, s[20:21]
	global_load_dwordx4 a[36:39], v14, s[22:23]
	global_load_dwordx4 a[40:43], v14, s[20:21] offset:1024
	global_load_dwordx4 a[44:47], v14, s[22:23] offset:1024
	global_load_dwordx4 a[48:51], v14, s[20:21] offset:2048
	global_load_dwordx4 a[52:55], v14, s[22:23] offset:2048
	global_load_dwordx4 a[56:59], v14, s[20:21] offset:3072
	global_load_dwordx4 a[60:63], v14, s[22:23] offset:3072
	global_load_dwordx4 a[64:67], v15, s[20:21]
	global_load_dwordx4 a[68:71], v15, s[22:23]
	global_load_dwordx4 a[72:75], v15, s[20:21] offset:1024
	global_load_dwordx4 a[76:79], v15, s[22:23] offset:1024
	global_load_dwordx4 a[80:83], v15, s[20:21] offset:2048
	global_load_dwordx4 a[84:87], v15, s[22:23] offset:2048
	global_load_dwordx4 a[88:91], v15, s[20:21] offset:3072
	global_load_dwordx4 a[92:95], v15, s[22:23] offset:3072
	global_load_dwordx4 a[96:99], v16, s[20:21]
	global_load_dwordx4 a[100:103], v16, s[22:23]
	global_load_dwordx4 a[104:107], v16, s[20:21] offset:1024
	global_load_dwordx4 a[108:111], v16, s[22:23] offset:1024
	global_load_dwordx4 a[112:115], v16, s[20:21] offset:2048
	global_load_dwordx4 a[116:119], v16, s[22:23] offset:2048
	global_load_dwordx4 a[120:123], v16, s[20:21] offset:3072
	global_load_dwordx4 a[124:127], v16, s[22:23] offset:3072
	global_load_dwordx4 a[128:131], v4, s[24:25]
	global_load_dwordx4 a[132:135], v4, s[24:25] offset:1024
	global_load_dwordx4 a[136:139], v4, s[24:25] offset:2048
	global_load_dwordx4 a[140:143], v4, s[24:25] offset:3072
	global_load_dwordx4 a[144:147], v14, s[24:25]
	global_load_dwordx4 a[148:151], v14, s[24:25] offset:1024
	global_load_dwordx4 a[152:155], v14, s[24:25] offset:2048
	global_load_dwordx4 a[156:159], v14, s[24:25] offset:3072
	global_load_dwordx4 a[160:163], v15, s[24:25]
	global_load_dwordx4 a[164:167], v15, s[24:25] offset:1024
	global_load_dwordx4 a[168:171], v15, s[24:25] offset:2048
	global_load_dwordx4 a[172:175], v15, s[24:25] offset:3072
	global_load_dwordx4 a[176:179], v16, s[24:25]
	global_load_dwordx4 a[180:183], v16, s[24:25] offset:1024
	global_load_dwordx4 a[184:187], v16, s[24:25] offset:2048
	global_load_dwordx4 a[188:191], v16, s[24:25] offset:3072
	s_mov_b32 s28, 0x3fb8aa3b
	s_mov_b32 s29, 0x3e4ccccd
	v_mov_b32_e32 v132, 0x3c003c00
	v_mov_b32_e32 v133, 0x3c003c00
	v_mov_b32_e32 v134, 0x3c003c00
	v_mov_b32_e32 v135, 0x3c003c00
	s_waitcnt vmcnt(54)
	v_max_f32_e32 v18, v28, v29
	v_max3_f32 v18, v18, v30, v31
	s_nop 1
	v_max_f32_dpp v18, v18, v18 quad_perm:[1,0,3,2] row_mask:0xf bank_mask:0xf
	s_nop 1
	v_max_f32_dpp v18, v18, v18 quad_perm:[2,3,0,1] row_mask:0xf bank_mask:0xf
	s_nop 1
	v_max_f32_dpp v18, v18, v18 row_half_mirror row_mask:0xf bank_mask:0xf
	s_nop 1
	v_max_f32_dpp v18, v18, v18 row_mirror row_mask:0xf bank_mask:0xf
	s_nop 1
	v_readlane_b32 s30, v18, 0
	v_readlane_b32 s31, v18, 16
	v_readlane_b32 s32, v18, 32
	v_readlane_b32 s33, v18, 48
	s_nop 3
	v_mov_b32_e32 v19, s30
	v_max_f32_e32 v19, s31, v19
	v_max_f32_e32 v19, s32, v19
	v_max_f32_e32 v19, s33, v19
	s_waitcnt vmcnt(53)
	v_sub_f32_e32 v20, v6, v19
	v_mul_f32_e32 v21, s29, v20
	v_mul_f32_e32 v20, s28, v20
	v_mul_f32_e32 v21, s28, v21
	v_exp_f32_e32 v20, v20
	v_exp_f32_e32 v21, v21
	s_waitcnt vmcnt(52)
	v_add_f32_e32 v22, v19, v7
	v_mul_f32_e32 v23, s29, v22
	v_max_f32_e32 v24, v22, v23
	v_sub_f32_e32 v22, v22, v24
	v_sub_f32_e32 v23, v23, v24
	v_mul_f32_e32 v22, s28, v22
	v_mul_f32_e32 v23, s28, v23
	ds_write_b32 v12, v20
	ds_write_b32 v12, v21 offset:1024
	v_exp_f32_e32 v24, v22
	v_exp_f32_e32 v26, v23
	s_waitcnt vmcnt(50)
	ds_write_b32 v12, v8 offset:2048
	ds_write_b32 v12, v9 offset:3072
	v_mov_b32_e32 v25, v24
	v_mov_b32_e32 v27, v26
	v_lshl_add_u32 v200, v5, 8, v3
	v_mov_b32_e32 v201, 21632
	v_lshl_add_u32 v201, v5, 12, v201
	v_add_u32_e32 v201, v201, v4
	v_add_u32_e32 v202, 21632, v4
	v_mov_b32_e32 v203, 4224
	v_lshl_add_u32 v203, v5, 7, v203
	v_lshl_add_u32 v203, v2, 2, v203
	v_mov_b32_e32 v204, 4224
	v_lshl_add_u32 v204, v2, 2, v204
	s_waitcnt lgkmcnt(0)
	s_barrier
	ds_read_b128 v[96:99], v200
	ds_read_b128 v[100:103], v200 offset:16
	ds_read_b128 v[104:107], v200 offset:1024
	ds_read_b128 v[108:111], v200 offset:1040
	s_waitcnt lgkmcnt(0)
	v_pk_mul_f32 v[112:113], v[96:97], v[24:25]
	v_pk_mul_f32 v[120:121], v[104:105], v[26:27]
	v_pk_mul_f32 v[114:115], v[98:99], v[24:25]
	v_pk_mul_f32 v[122:123], v[106:107], v[26:27]
	v_pk_mul_f32 v[116:117], v[100:101], v[24:25]
	v_pk_mul_f32 v[124:125], v[108:109], v[26:27]
	v_pk_mul_f32 v[118:119], v[102:103], v[24:25]
	v_pk_mul_f32 v[126:127], v[110:111], v[26:27]
	v_max_f32_e32 v112, v112, v120
	v_max_f32_e32 v113, v113, v121
	v_max_f32_e32 v114, v114, v122
	v_max_f32_e32 v115, v115, v123
	v_max_f32_e32 v116, v116, v124
	v_max_f32_e32 v117, v117, v125
	v_max_f32_e32 v118, v118, v126
	v_max_f32_e32 v119, v119, v127
	v_cvt_pk_f16_f32 v128, v112, v113
	v_cvt_pk_f16_f32 v129, v114, v115
	v_cvt_pk_f16_f32 v130, v116, v117
	v_cvt_pk_f16_f32 v131, v118, v119
	ds_write_b128 v201, v[128:131]
	s_nop 0
	v_mfma_f32_32x32x16_f16 v[80:95], v[132:135], v[128:131], 0
	ds_read_b128 v[96:99], v200 offset:64
	ds_read_b128 v[100:103], v200 offset:80
	ds_read_b128 v[104:107], v200 offset:1088
	ds_read_b128 v[108:111], v200 offset:1104
	s_waitcnt lgkmcnt(0)
	v_pk_mul_f32 v[112:113], v[96:97], v[24:25]
	v_pk_mul_f32 v[120:121], v[104:105], v[26:27]
	v_pk_mul_f32 v[114:115], v[98:99], v[24:25]
	v_pk_mul_f32 v[122:123], v[106:107], v[26:27]
	v_pk_mul_f32 v[116:117], v[100:101], v[24:25]
	v_pk_mul_f32 v[124:125], v[108:109], v[26:27]
	v_pk_mul_f32 v[118:119], v[102:103], v[24:25]
	v_pk_mul_f32 v[126:127], v[110:111], v[26:27]
	v_max_f32_e32 v112, v112, v120
	v_max_f32_e32 v113, v113, v121
	v_max_f32_e32 v114, v114, v122
	v_max_f32_e32 v115, v115, v123
	v_max_f32_e32 v116, v116, v124
	v_max_f32_e32 v117, v117, v125
	v_max_f32_e32 v118, v118, v126
	v_max_f32_e32 v119, v119, v127
	v_cvt_pk_f16_f32 v128, v112, v113
	v_cvt_pk_f16_f32 v129, v114, v115
	v_cvt_pk_f16_f32 v130, v116, v117
	v_cvt_pk_f16_f32 v131, v118, v119
	ds_write_b128 v201, v[128:131] offset:1024
	s_nop 0
	v_mfma_f32_32x32x16_f16 v[80:95], v[132:135], v[128:131], v[80:95]
	ds_read_b128 v[96:99], v200 offset:128
	ds_read_b128 v[100:103], v200 offset:144
	ds_read_b128 v[104:107], v200 offset:1152
	ds_read_b128 v[108:111], v200 offset:1168
	s_waitcnt lgkmcnt(0)
	v_pk_mul_f32 v[112:113], v[96:97], v[24:25]
	v_pk_mul_f32 v[120:121], v[104:105], v[26:27]
	v_pk_mul_f32 v[114:115], v[98:99], v[24:25]
	v_pk_mul_f32 v[122:123], v[106:107], v[26:27]
	v_pk_mul_f32 v[116:117], v[100:101], v[24:25]
	v_pk_mul_f32 v[124:125], v[108:109], v[26:27]
	v_pk_mul_f32 v[118:119], v[102:103], v[24:25]
	v_pk_mul_f32 v[126:127], v[110:111], v[26:27]
	v_max_f32_e32 v112, v112, v120
	v_max_f32_e32 v113, v113, v121
	v_max_f32_e32 v114, v114, v122
	v_max_f32_e32 v115, v115, v123
	v_max_f32_e32 v116, v116, v124
	v_max_f32_e32 v117, v117, v125
	v_max_f32_e32 v118, v118, v126
	v_max_f32_e32 v119, v119, v127
	v_cvt_pk_f16_f32 v128, v112, v113
	v_cvt_pk_f16_f32 v129, v114, v115
	v_cvt_pk_f16_f32 v130, v116, v117
	v_cvt_pk_f16_f32 v131, v118, v119
	ds_write_b128 v201, v[128:131] offset:2048
	s_nop 0
	v_mfma_f32_32x32x16_f16 v[80:95], v[132:135], v[128:131], v[80:95]
	ds_read_b128 v[96:99], v200 offset:192
	ds_read_b128 v[100:103], v200 offset:208
	ds_read_b128 v[104:107], v200 offset:1216
	ds_read_b128 v[108:111], v200 offset:1232
	s_waitcnt lgkmcnt(0)
	v_pk_mul_f32 v[112:113], v[96:97], v[24:25]
	v_pk_mul_f32 v[120:121], v[104:105], v[26:27]
	v_pk_mul_f32 v[114:115], v[98:99], v[24:25]
	v_pk_mul_f32 v[122:123], v[106:107], v[26:27]
	v_pk_mul_f32 v[116:117], v[100:101], v[24:25]
	v_pk_mul_f32 v[124:125], v[108:109], v[26:27]
	v_pk_mul_f32 v[118:119], v[102:103], v[24:25]
	v_pk_mul_f32 v[126:127], v[110:111], v[26:27]
	v_max_f32_e32 v112, v112, v120
	v_max_f32_e32 v113, v113, v121
	v_max_f32_e32 v114, v114, v122
	v_max_f32_e32 v115, v115, v123
	v_max_f32_e32 v116, v116, v124
	v_max_f32_e32 v117, v117, v125
	v_max_f32_e32 v118, v118, v126
	v_max_f32_e32 v119, v119, v127
	v_cvt_pk_f16_f32 v128, v112, v113
	v_cvt_pk_f16_f32 v129, v114, v115
	v_cvt_pk_f16_f32 v130, v116, v117
	v_cvt_pk_f16_f32 v131, v118, v119
	ds_write_b128 v201, v[128:131] offset:3072
	s_nop 0
	v_mfma_f32_32x32x16_f16 v[80:95], v[132:135], v[128:131], v[80:95]
	s_nop 15
	ds_write_b32 v203, v80
	s_waitcnt lgkmcnt(0)
	s_barrier
	ds_read_b32 v205, v204
	ds_read_b32 v206, v204 offset:128
	ds_read_b32 v207, v204 offset:256
	ds_read_b32 v208, v204 offset:384
	ds_read_b128 v[136:139], v202
	ds_read_b128 v[140:143], v202 offset:1024
	s_waitcnt lgkmcnt(1)
	s_waitcnt vmcnt(46)
	v_mfma_f32_32x32x16_f16 v[32:47], v[136:139], a[0:3], 0
	v_mfma_f32_32x32x16_f16 v[48:63], v[136:139], a[4:7], 0
	ds_read_b128 v[136:139], v202 offset:2048
	s_waitcnt lgkmcnt(1)
	s_waitcnt vmcnt(44)
	v_mfma_f32_32x32x16_f16 v[32:47], v[140:143], a[8:11], v[32:47]
	v_mfma_f32_32x32x16_f16 v[48:63], v[140:143], a[12:15], v[48:63]
	v_add_f32_e32 v205, v205, v206
	v_add_f32_e32 v205, v205, v207
	v_add_f32_e32 v205, v205, v208
	v_div_scale_f32 v206, s[34:35], v205, v205, 1.0
	v_rcp_f32_e32 v207, v206
	s_nop 0
	v_fma_f32 v208, -v206, v207, 1.0
	v_fmac_f32_e32 v207, v208, v207
	v_div_scale_f32 v208, vcc, 1.0, v205, 1.0
	v_mul_f32_e32 v209, v208, v207
	v_fma_f32 v210, -v206, v209, v208
	v_fmac_f32_e32 v209, v210, v207
	v_fma_f32 v208, -v206, v209, v208
	v_div_fmas_f32 v208, v208, v207, v209
	v_div_fixup_f32 v208, v208, v205, 1.0
	ds_read_b128 v[140:143], v202 offset:3072
	s_waitcnt lgkmcnt(1)
	s_waitcnt vmcnt(42)
	v_mfma_f32_32x32x16_f16 v[32:47], v[136:139], a[16:19], v[32:47]
	v_mfma_f32_32x32x16_f16 v[48:63], v[136:139], a[20:23], v[48:63]
	ds_read_b128 v[136:139], v202 offset:4096
	s_waitcnt lgkmcnt(1)
	s_waitcnt vmcnt(40)
	v_mfma_f32_32x32x16_f16 v[32:47], v[140:143], a[24:27], v[32:47]
	v_mfma_f32_32x32x16_f16 v[48:63], v[140:143], a[28:31], v[48:63]
	ds_read_b128 v[140:143], v202 offset:5120
	s_waitcnt lgkmcnt(1)
	s_waitcnt vmcnt(38)
	v_mfma_f32_32x32x16_f16 v[32:47], v[136:139], a[32:35], v[32:47]
	v_mfma_f32_32x32x16_f16 v[48:63], v[136:139], a[36:39], v[48:63]
	ds_read_b128 v[136:139], v202 offset:6144
	s_waitcnt lgkmcnt(1)
	s_waitcnt vmcnt(36)
	v_mfma_f32_32x32x16_f16 v[32:47], v[140:143], a[40:43], v[32:47]
	v_mfma_f32_32x32x16_f16 v[48:63], v[140:143], a[44:47], v[48:63]
	ds_read_b128 v[140:143], v202 offset:7168
	s_waitcnt lgkmcnt(1)
	s_waitcnt vmcnt(34)
	v_mfma_f32_32x32x16_f16 v[32:47], v[136:139], a[48:51], v[32:47]
	v_mfma_f32_32x32x16_f16 v[48:63], v[136:139], a[52:55], v[48:63]
	ds_read_b128 v[136:139], v202 offset:8192
	s_waitcnt lgkmcnt(1)
	s_waitcnt vmcnt(32)
	v_mfma_f32_32x32x16_f16 v[32:47], v[140:143], a[56:59], v[32:47]
	v_mfma_f32_32x32x16_f16 v[48:63], v[140:143], a[60:63], v[48:63]
	ds_read_b128 v[140:143], v202 offset:9216
	s_waitcnt lgkmcnt(1)
	s_waitcnt vmcnt(30)
	v_mfma_f32_32x32x16_f16 v[32:47], v[136:139], a[64:67], v[32:47]
	v_mfma_f32_32x32x16_f16 v[48:63], v[136:139], a[68:71], v[48:63]
	ds_read_b128 v[136:139], v202 offset:10240
	s_waitcnt lgkmcnt(1)
	s_waitcnt vmcnt(28)
	v_mfma_f32_32x32x16_f16 v[32:47], v[140:143], a[72:75], v[32:47]
	v_mfma_f32_32x32x16_f16 v[48:63], v[140:143], a[76:79], v[48:63]
	ds_read_b128 v[140:143], v202 offset:11264
	s_waitcnt lgkmcnt(1)
	s_waitcnt vmcnt(26)
	v_mfma_f32_32x32x16_f16 v[32:47], v[136:139], a[80:83], v[32:47]
	v_mfma_f32_32x32x16_f16 v[48:63], v[136:139], a[84:87], v[48:63]
	ds_read_b128 v[136:139], v202 offset:12288
	s_waitcnt lgkmcnt(1)
	s_waitcnt vmcnt(24)
	v_mfma_f32_32x32x16_f16 v[32:47], v[140:143], a[88:91], v[32:47]
	v_mfma_f32_32x32x16_f16 v[48:63], v[140:143], a[92:95], v[48:63]
	ds_read_b128 v[140:143], v202 offset:13312
	s_waitcnt lgkmcnt(1)
	s_waitcnt vmcnt(22)
	v_mfma_f32_32x32x16_f16 v[32:47], v[136:139], a[96:99], v[32:47]
	v_mfma_f32_32x32x16_f16 v[48:63], v[136:139], a[100:103], v[48:63]
	ds_read_b128 v[136:139], v202 offset:14336
	s_waitcnt lgkmcnt(1)
	s_waitcnt vmcnt(20)
	v_mfma_f32_32x32x16_f16 v[32:47], v[140:143], a[104:107], v[32:47]
	v_mfma_f32_32x32x16_f16 v[48:63], v[140:143], a[108:111], v[48:63]
	ds_read_b128 v[140:143], v202 offset:15360
	s_waitcnt lgkmcnt(1)
	s_waitcnt vmcnt(18)
	v_mfma_f32_32x32x16_f16 v[32:47], v[136:139], a[112:115], v[32:47]
	v_mfma_f32_32x32x16_f16 v[48:63], v[136:139], a[116:119], v[48:63]
	s_waitcnt lgkmcnt(0)
	s_waitcnt vmcnt(16)
	v_mfma_f32_32x32x16_f16 v[32:47], v[140:143], a[120:123], v[32:47]
	v_mfma_f32_32x32x16_f16 v[48:63], v[140:143], a[124:127], v[48:63]
	v_lshrrev_b32_e32 v211, 1, v3
	ds_bpermute_b32 v144, v211, v208
	ds_bpermute_b32 v145, v211, v208 offset:4
	ds_bpermute_b32 v146, v211, v208 offset:8
	ds_bpermute_b32 v147, v211, v208 offset:12
	ds_bpermute_b32 v148, v211, v208 offset:32
	ds_bpermute_b32 v149, v211, v208 offset:36
	ds_bpermute_b32 v150, v211, v208 offset:40
	ds_bpermute_b32 v151, v211, v208 offset:44
	ds_bpermute_b32 v152, v211, v208 offset:64
	ds_bpermute_b32 v153, v211, v208 offset:68
	ds_bpermute_b32 v154, v211, v208 offset:72
	ds_bpermute_b32 v155, v211, v208 offset:76
	ds_bpermute_b32 v156, v211, v208 offset:96
	ds_bpermute_b32 v157, v211, v208 offset:100
	ds_bpermute_b32 v158, v211, v208 offset:104
	ds_bpermute_b32 v159, v211, v208 offset:108
	v_mov_b32_e32 v212, 4736
	v_lshrrev_b32_e32 v213, 5, v3
	s_movk_i32 s38, 0x840
	v_mad_u32_u24 v212, v213, s38, v212
	v_lshl_add_u32 v212, v5, 7, v212
	v_lshl_add_u32 v212, v2, 1, v212
	s_waitcnt vmcnt(16)
	s_waitcnt lgkmcnt(0)
	s_nop 4
	v_fma_f32 v160, v32, v144, v10
	v_fma_f32 v161, v33, v145, v10
	v_fma_f32 v162, v34, v146, v10
	v_fma_f32 v163, v35, v147, v10
	v_fma_f32 v164, v36, v148, v10
	v_fma_f32 v165, v37, v149, v10
	v_fma_f32 v166, v38, v150, v10
	v_fma_f32 v167, v39, v151, v10
	v_fma_f32 v168, v40, v152, v10
	v_fma_f32 v169, v41, v153, v10
	v_fma_f32 v170, v42, v154, v10
	v_fma_f32 v171, v43, v155, v10
	v_fma_f32 v172, v44, v156, v10
	v_fma_f32 v173, v45, v157, v10
	v_fma_f32 v174, v46, v158, v10
	v_fma_f32 v175, v47, v159, v10
	v_max_f32_e32 v160, 0, v160
	v_max_f32_e32 v161, 0, v161
	v_max_f32_e32 v162, 0, v162
	v_max_f32_e32 v163, 0, v163
	v_max_f32_e32 v164, 0, v164
	v_max_f32_e32 v165, 0, v165
	v_max_f32_e32 v166, 0, v166
	v_max_f32_e32 v167, 0, v167
	v_max_f32_e32 v168, 0, v168
	v_max_f32_e32 v169, 0, v169
	v_max_f32_e32 v170, 0, v170
	v_max_f32_e32 v171, 0, v171
	v_max_f32_e32 v172, 0, v172
	v_max_f32_e32 v173, 0, v173
	v_max_f32_e32 v174, 0, v174
	v_max_f32_e32 v175, 0, v175
	v_cvt_f16_f32_e32 v160, v160
	v_cvt_f16_f32_e32 v161, v161
	v_cvt_f16_f32_e32 v162, v162
	v_cvt_f16_f32_e32 v163, v163
	v_cvt_f16_f32_e32 v164, v164
	v_cvt_f16_f32_e32 v165, v165
	v_cvt_f16_f32_e32 v166, v166
	v_cvt_f16_f32_e32 v167, v167
	v_cvt_f16_f32_e32 v168, v168
	v_cvt_f16_f32_e32 v169, v169
	v_cvt_f16_f32_e32 v170, v170
	v_cvt_f16_f32_e32 v171, v171
	v_cvt_f16_f32_e32 v172, v172
	v_cvt_f16_f32_e32 v173, v173
	v_cvt_f16_f32_e32 v174, v174
	v_cvt_f16_f32_e32 v175, v175
	ds_write_b16 v212, v160
	ds_write_b16 v212, v161 offset:528
	ds_write_b16 v212, v162 offset:1056
	ds_write_b16 v212, v163 offset:1584
	ds_write_b16 v212, v164 offset:4224
	ds_write_b16 v212, v165 offset:4752
	ds_write_b16 v212, v166 offset:5280
	ds_write_b16 v212, v167 offset:5808
	ds_write_b16 v212, v168 offset:8448
	ds_write_b16 v212, v169 offset:8976
	ds_write_b16 v212, v170 offset:9504
	ds_write_b16 v212, v171 offset:10032
	ds_write_b16 v212, v172 offset:12672
	ds_write_b16 v212, v173 offset:13200
	ds_write_b16 v212, v174 offset:13728
	ds_write_b16 v212, v175 offset:14256
	v_fma_f32 v160, v48, v144, v11
	v_fma_f32 v161, v49, v145, v11
	v_fma_f32 v162, v50, v146, v11
	v_fma_f32 v163, v51, v147, v11
	v_fma_f32 v164, v52, v148, v11
	v_fma_f32 v165, v53, v149, v11
	v_fma_f32 v166, v54, v150, v11
	v_fma_f32 v167, v55, v151, v11
	v_fma_f32 v168, v56, v152, v11
	v_fma_f32 v169, v57, v153, v11
	v_fma_f32 v170, v58, v154, v11
	v_fma_f32 v171, v59, v155, v11
	v_fma_f32 v172, v60, v156, v11
	v_fma_f32 v173, v61, v157, v11
	v_fma_f32 v174, v62, v158, v11
	v_fma_f32 v175, v63, v159, v11
	v_max_f32_e32 v160, 0, v160
	v_max_f32_e32 v161, 0, v161
	v_max_f32_e32 v162, 0, v162
	v_max_f32_e32 v163, 0, v163
	v_max_f32_e32 v164, 0, v164
	v_max_f32_e32 v165, 0, v165
	v_max_f32_e32 v166, 0, v166
	v_max_f32_e32 v167, 0, v167
	v_max_f32_e32 v168, 0, v168
	v_max_f32_e32 v169, 0, v169
	v_max_f32_e32 v170, 0, v170
	v_max_f32_e32 v171, 0, v171
	v_max_f32_e32 v172, 0, v172
	v_max_f32_e32 v173, 0, v173
	v_max_f32_e32 v174, 0, v174
	v_max_f32_e32 v175, 0, v175
	v_cvt_f16_f32_e32 v160, v160
	v_cvt_f16_f32_e32 v161, v161
	v_cvt_f16_f32_e32 v162, v162
	v_cvt_f16_f32_e32 v163, v163
	v_cvt_f16_f32_e32 v164, v164
	v_cvt_f16_f32_e32 v165, v165
	v_cvt_f16_f32_e32 v166, v166
	v_cvt_f16_f32_e32 v167, v167
	v_cvt_f16_f32_e32 v168, v168
	v_cvt_f16_f32_e32 v169, v169
	v_cvt_f16_f32_e32 v170, v170
	v_cvt_f16_f32_e32 v171, v171
	v_cvt_f16_f32_e32 v172, v172
	v_cvt_f16_f32_e32 v173, v173
	v_cvt_f16_f32_e32 v174, v174
	v_cvt_f16_f32_e32 v175, v175
	ds_write_b16 v212, v160 offset:64
	ds_write_b16 v212, v161 offset:592
	ds_write_b16 v212, v162 offset:1120
	ds_write_b16 v212, v163 offset:1648
	ds_write_b16 v212, v164 offset:4288
	ds_write_b16 v212, v165 offset:4816
	ds_write_b16 v212, v166 offset:5344
	ds_write_b16 v212, v167 offset:5872
	ds_write_b16 v212, v168 offset:8512
	ds_write_b16 v212, v169 offset:9040
	ds_write_b16 v212, v170 offset:9568
	ds_write_b16 v212, v171 offset:10096
	ds_write_b16 v212, v172 offset:12736
	ds_write_b16 v212, v173 offset:13264
	ds_write_b16 v212, v174 offset:13792
	ds_write_b16 v212, v175 offset:14320
	s_waitcnt lgkmcnt(0)
	s_barrier
	v_lshrrev_b32_e32 v213, 3, v0
	v_and_b32_e32 v214, 7, v0
	v_mov_b32_e32 v215, 4736
	s_movk_i32 s39, 0x210
	v_mad_u32_u24 v215, v213, s39, v215
	v_lshl_add_u32 v215, v214, 6, v215
	v_lshlrev_b32_e32 v216, 7, v214
	v_mov_b32_e32 v217, 4736
	v_mad_u32_u24 v217, v2, s39, v217
	v_lshrrev_b32_e32 v218, 1, v3
	v_add_u32_e32 v217, v217, v218
	ds_read_b128 v[176:179], v215
	ds_read_b128 v[180:183], v215 offset:16
	ds_read_b128 v[184:187], v215 offset:32
	ds_read_b128 v[188:191], v215 offset:48
	ds_read_b128 v[32:35], v216 offset:2048
	ds_read_b128 v[36:39], v216 offset:2064
	ds_read_b128 v[40:43], v216 offset:2080
	ds_read_b128 v[44:47], v216 offset:2096
	ds_read_b128 v[48:51], v216 offset:2112
	ds_read_b128 v[52:55], v216 offset:2128
	ds_read_b128 v[56:59], v216 offset:2144
	ds_read_b128 v[60:63], v216 offset:2160
	ds_read_b128 v[136:139], v217
	v_mov_b32_e32 v28, 0
	v_mov_b32_e32 v29, 0
	ds_read_b128 v[140:143], v217 offset:32
	s_waitcnt lgkmcnt(1)
	ds_read_b128 v[96:99], v216 offset:3072
	ds_read_b128 v[100:103], v216 offset:3088
	ds_read_b128 v[104:107], v216 offset:3104
	ds_read_b128 v[108:111], v216 offset:3120
	ds_read_b128 v[112:115], v216 offset:3136
	ds_read_b128 v[116:119], v216 offset:3152
	ds_read_b128 v[120:123], v216 offset:3168
	ds_read_b128 v[124:127], v216 offset:3184
	s_waitcnt vmcnt(15)
	v_mfma_f32_32x32x16_f16 v[64:79], v[136:139], a[128:131], 0
	v_fma_mix_f32 v28, v32, v176, v28 op_sel_hi:[0,1,0]
	v_fma_mix_f32 v28, v33, v176, v28 op_sel:[0,1,0] op_sel_hi:[0,1,0]
	v_fma_mix_f32 v28, v34, v177, v28 op_sel_hi:[0,1,0]
	v_fma_mix_f32 v28, v35, v177, v28 op_sel:[0,1,0] op_sel_hi:[0,1,0]
	v_fma_mix_f32 v28, v36, v178, v28 op_sel_hi:[0,1,0]
	v_fma_mix_f32 v28, v37, v178, v28 op_sel:[0,1,0] op_sel_hi:[0,1,0]
	v_fma_mix_f32 v28, v38, v179, v28 op_sel_hi:[0,1,0]
	v_fma_mix_f32 v28, v39, v179, v28 op_sel:[0,1,0] op_sel_hi:[0,1,0]
	ds_read_b128 v[136:139], v217 offset:64
	s_waitcnt lgkmcnt(1)
	s_waitcnt vmcnt(14)
	v_mfma_f32_32x32x16_f16 v[64:79], v[140:143], a[132:135], v[64:79]
	v_fma_mix_f32 v28, v40, v180, v28 op_sel_hi:[0,1,0]
	v_fma_mix_f32 v28, v41, v180, v28 op_sel:[0,1,0] op_sel_hi:[0,1,0]
	v_fma_mix_f32 v28, v42, v181, v28 op_sel_hi:[0,1,0]
	v_fma_mix_f32 v28, v43, v181, v28 op_sel:[0,1,0] op_sel_hi:[0,1,0]
	v_fma_mix_f32 v28, v44, v182, v28 op_sel_hi:[0,1,0]
	v_fma_mix_f32 v28, v45, v182, v28 op_sel:[0,1,0] op_sel_hi:[0,1,0]
	v_fma_mix_f32 v28, v46, v183, v28 op_sel_hi:[0,1,0]
	v_fma_mix_f32 v28, v47, v183, v28 op_sel:[0,1,0] op_sel_hi:[0,1,0]
	ds_read_b128 v[140:143], v217 offset:96
	s_waitcnt lgkmcnt(1)
	s_waitcnt vmcnt(13)
	v_mfma_f32_32x32x16_f16 v[64:79], v[136:139], a[136:139], v[64:79]
	v_fma_mix_f32 v28, v48, v184, v28 op_sel_hi:[0,1,0]
	v_fma_mix_f32 v28, v49, v184, v28 op_sel:[0,1,0] op_sel_hi:[0,1,0]
	v_fma_mix_f32 v28, v50, v185, v28 op_sel_hi:[0,1,0]
	v_fma_mix_f32 v28, v51, v185, v28 op_sel:[0,1,0] op_sel_hi:[0,1,0]
	v_fma_mix_f32 v28, v52, v186, v28 op_sel_hi:[0,1,0]
	v_fma_mix_f32 v28, v53, v186, v28 op_sel:[0,1,0] op_sel_hi:[0,1,0]
	v_fma_mix_f32 v28, v54, v187, v28 op_sel_hi:[0,1,0]
	v_fma_mix_f32 v28, v55, v187, v28 op_sel:[0,1,0] op_sel_hi:[0,1,0]
	ds_read_b128 v[136:139], v217 offset:128
	s_waitcnt lgkmcnt(1)
	s_waitcnt vmcnt(12)
	v_mfma_f32_32x32x16_f16 v[64:79], v[140:143], a[140:143], v[64:79]
	v_fma_mix_f32 v28, v56, v188, v28 op_sel_hi:[0,1,0]
	v_fma_mix_f32 v28, v57, v188, v28 op_sel:[0,1,0] op_sel_hi:[0,1,0]
	v_fma_mix_f32 v28, v58, v189, v28 op_sel_hi:[0,1,0]
	v_fma_mix_f32 v28, v59, v189, v28 op_sel:[0,1,0] op_sel_hi:[0,1,0]
	v_fma_mix_f32 v28, v60, v190, v28 op_sel_hi:[0,1,0]
	v_fma_mix_f32 v28, v61, v190, v28 op_sel:[0,1,0] op_sel_hi:[0,1,0]
	v_fma_mix_f32 v28, v62, v191, v28 op_sel_hi:[0,1,0]
	v_fma_mix_f32 v28, v63, v191, v28 op_sel:[0,1,0] op_sel_hi:[0,1,0]
	ds_read_b128 v[140:143], v217 offset:160
	s_waitcnt lgkmcnt(1)
	s_waitcnt vmcnt(11)
	v_mfma_f32_32x32x16_f16 v[64:79], v[136:139], a[144:147], v[64:79]
	v_fma_mix_f32 v29, v96, v176, v29 op_sel_hi:[0,1,0]
	v_fma_mix_f32 v29, v97, v176, v29 op_sel:[0,1,0] op_sel_hi:[0,1,0]
	v_fma_mix_f32 v29, v98, v177, v29 op_sel_hi:[0,1,0]
	v_fma_mix_f32 v29, v99, v177, v29 op_sel:[0,1,0] op_sel_hi:[0,1,0]
	v_fma_mix_f32 v29, v100, v178, v29 op_sel_hi:[0,1,0]
	v_fma_mix_f32 v29, v101, v178, v29 op_sel:[0,1,0] op_sel_hi:[0,1,0]
	v_fma_mix_f32 v29, v102, v179, v29 op_sel_hi:[0,1,0]
	v_fma_mix_f32 v29, v103, v179, v29 op_sel:[0,1,0] op_sel_hi:[0,1,0]
	ds_read_b128 v[136:139], v217 offset:192
	s_waitcnt lgkmcnt(1)
	s_waitcnt vmcnt(10)
	v_mfma_f32_32x32x16_f16 v[64:79], v[140:143], a[148:151], v[64:79]
	v_fma_mix_f32 v29, v104, v180, v29 op_sel_hi:[0,1,0]
	v_fma_mix_f32 v29, v105, v180, v29 op_sel:[0,1,0] op_sel_hi:[0,1,0]
	v_fma_mix_f32 v29, v106, v181, v29 op_sel_hi:[0,1,0]
	v_fma_mix_f32 v29, v107, v181, v29 op_sel:[0,1,0] op_sel_hi:[0,1,0]
	v_fma_mix_f32 v29, v108, v182, v29 op_sel_hi:[0,1,0]
	v_fma_mix_f32 v29, v109, v182, v29 op_sel:[0,1,0] op_sel_hi:[0,1,0]
	v_fma_mix_f32 v29, v110, v183, v29 op_sel_hi:[0,1,0]
	v_fma_mix_f32 v29, v111, v183, v29 op_sel:[0,1,0] op_sel_hi:[0,1,0]
	ds_read_b128 v[140:143], v217 offset:224
	s_waitcnt lgkmcnt(1)
	s_waitcnt vmcnt(9)
	v_mfma_f32_32x32x16_f16 v[64:79], v[136:139], a[152:155], v[64:79]
	v_fma_mix_f32 v29, v112, v184, v29 op_sel_hi:[0,1,0]
	v_fma_mix_f32 v29, v113, v184, v29 op_sel:[0,1,0] op_sel_hi:[0,1,0]
	v_fma_mix_f32 v29, v114, v185, v29 op_sel_hi:[0,1,0]
	v_fma_mix_f32 v29, v115, v185, v29 op_sel:[0,1,0] op_sel_hi:[0,1,0]
	v_fma_mix_f32 v29, v116, v186, v29 op_sel_hi:[0,1,0]
	v_fma_mix_f32 v29, v117, v186, v29 op_sel:[0,1,0] op_sel_hi:[0,1,0]
	v_fma_mix_f32 v29, v118, v187, v29 op_sel_hi:[0,1,0]
	v_fma_mix_f32 v29, v119, v187, v29 op_sel:[0,1,0] op_sel_hi:[0,1,0]
	ds_read_b128 v[136:139], v217 offset:256
	s_waitcnt lgkmcnt(1)
	s_waitcnt vmcnt(8)
	v_mfma_f32_32x32x16_f16 v[64:79], v[140:143], a[156:159], v[64:79]
	v_fma_mix_f32 v29, v120, v188, v29 op_sel_hi:[0,1,0]
	v_fma_mix_f32 v29, v121, v188, v29 op_sel:[0,1,0] op_sel_hi:[0,1,0]
	v_fma_mix_f32 v29, v122, v189, v29 op_sel_hi:[0,1,0]
	v_fma_mix_f32 v29, v123, v189, v29 op_sel:[0,1,0] op_sel_hi:[0,1,0]
	v_fma_mix_f32 v29, v124, v190, v29 op_sel_hi:[0,1,0]
	v_fma_mix_f32 v29, v125, v190, v29 op_sel:[0,1,0] op_sel_hi:[0,1,0]
	v_fma_mix_f32 v29, v126, v191, v29 op_sel_hi:[0,1,0]
	v_fma_mix_f32 v29, v127, v191, v29 op_sel:[0,1,0] op_sel_hi:[0,1,0]
	ds_read_b128 v[140:143], v217 offset:288
	s_waitcnt lgkmcnt(1)
	s_waitcnt vmcnt(7)
	v_mfma_f32_32x32x16_f16 v[64:79], v[136:139], a[160:163], v[64:79]
	ds_read_b128 v[136:139], v217 offset:320
	s_waitcnt lgkmcnt(1)
	s_waitcnt vmcnt(6)
	v_mfma_f32_32x32x16_f16 v[64:79], v[140:143], a[164:167], v[64:79]
	ds_read_b128 v[140:143], v217 offset:352
	s_waitcnt lgkmcnt(1)
	s_waitcnt vmcnt(5)
	v_mfma_f32_32x32x16_f16 v[64:79], v[136:139], a[168:171], v[64:79]
	ds_read_b128 v[136:139], v217 offset:384
	s_waitcnt lgkmcnt(1)
	s_waitcnt vmcnt(4)
	v_mfma_f32_32x32x16_f16 v[64:79], v[140:143], a[172:175], v[64:79]
	ds_read_b128 v[140:143], v217 offset:416
	s_waitcnt lgkmcnt(1)
	s_waitcnt vmcnt(3)
	v_mfma_f32_32x32x16_f16 v[64:79], v[136:139], a[176:179], v[64:79]
	ds_read_b128 v[136:139], v217 offset:448
	s_waitcnt lgkmcnt(1)
	s_waitcnt vmcnt(2)
	v_mfma_f32_32x32x16_f16 v[64:79], v[140:143], a[180:183], v[64:79]
	ds_read_b128 v[140:143], v217 offset:480
	s_waitcnt lgkmcnt(1)
	s_waitcnt vmcnt(1)
	v_mfma_f32_32x32x16_f16 v[64:79], v[136:139], a[184:187], v[64:79]
	s_waitcnt lgkmcnt(0)
	s_waitcnt vmcnt(0)
	v_mfma_f32_32x32x16_f16 v[64:79], v[140:143], a[188:191], v[64:79]
	s_nop 1
	v_add_f32_dpp v28, v28, v28 quad_perm:[1,0,3,2] row_mask:0xf bank_mask:0xf
	v_add_f32_dpp v29, v29, v29 quad_perm:[1,0,3,2] row_mask:0xf bank_mask:0xf
	s_nop 1
	v_add_f32_dpp v28, v28, v28 quad_perm:[2,3,0,1] row_mask:0xf bank_mask:0xf
	v_add_f32_dpp v29, v29, v29 quad_perm:[2,3,0,1] row_mask:0xf bank_mask:0xf
	s_nop 1
	v_add_f32_dpp v28, v28, v28 row_half_mirror row_mask:0xf bank_mask:0xf
	v_add_f32_dpp v29, v29, v29 row_half_mirror row_mask:0xf bank_mask:0xf
	s_nop 1
	v_add_u32_e32 v213, s18, v213
	v_lshlrev_b32_e32 v213, 2, v213
	v_cmp_eq_u32_e32 vcc, 0, v214
	s_and_saveexec_b64 s[34:35], vcc
	global_store_dword v213, v28, s[16:17]
	global_store_dword v213, v29, s[16:17] offset:1024
	s_mov_b64 exec, s[34:35]
	s_lshl_b32 s36, s2, 11
	s_add_u32 s36, s36, s27
	s_add_u32 s36, s14, s36
	s_addc_u32 s37, s15, 0
	v_lshrrev_b32_e32 v219, 2, v3
	v_lshl_add_u32 v219, v2, 4, v219
	s_nop 7
	v_cvt_pk_f16_f32 v220, v64, v65
	v_cvt_pk_f16_f32 v221, v66, v67
	v_cvt_pk_f16_f32 v222, v68, v69
	v_cvt_pk_f16_f32 v223, v70, v71
	v_cvt_pk_f16_f32 v224, v72, v73
	v_cvt_pk_f16_f32 v225, v74, v75
	v_cvt_pk_f16_f32 v226, v76, v77
	v_cvt_pk_f16_f32 v227, v78, v79
	global_store_dwordx2 v219, v[220:221], s[36:37]
	global_store_dwordx2 v219, v[222:223], s[36:37] offset:512
	global_store_dwordx2 v219, v[224:225], s[36:37] offset:1024
	global_store_dwordx2 v219, v[226:227], s[36:37] offset:1536
	s_endpgm

	.amdhsa_kernel _Z11gat2_kernelPKfPKDF16_S0_S2_S0_PDF16_PfS2_S2_S0_S4_
		.amdhsa_group_segment_fixed_size 38016
		.amdhsa_private_segment_fixed_size 0
		.amdhsa_kernarg_size 88
		.amdhsa_user_sgpr_count 2
		.amdhsa_user_sgpr_dispatch_ptr 0
		.amdhsa_user_sgpr_queue_ptr 0
		.amdhsa_user_sgpr_kernarg_segment_ptr 1
		.amdhsa_user_sgpr_dispatch_id 0
		.amdhsa_user_sgpr_kernarg_preload_length 0
		.amdhsa_user_sgpr_kernarg_preload_offset 0
		.amdhsa_user_sgpr_private_segment_size 0
		.amdhsa_uses_dynamic_stack 0
		.amdhsa_enable_private_segment 0
		.amdhsa_system_sgpr_workgroup_id_x 1
		.amdhsa_system_sgpr_workgroup_id_y 0
		.amdhsa_system_sgpr_workgroup_id_z 0
		.amdhsa_system_sgpr_workgroup_info 0
		.amdhsa_system_vgpr_workitem_id 0
		.amdhsa_next_free_vgpr 424
		.amdhsa_next_free_sgpr 96
		.amdhsa_accum_offset 232
		.amdhsa_reserve_vcc 1
		.amdhsa_float_round_mode_32 0
		.amdhsa_float_round_mode_16_64 0
		.amdhsa_float_denorm_mode_32 3
		.amdhsa_float_denorm_mode_16_64 3
		.amdhsa_dx10_clamp 1
		.amdhsa_ieee_mode 1
		.amdhsa_fp16_overflow 0
		.amdhsa_tg_split 0
		.amdhsa_exception_fp_ieee_invalid_op 0
		.amdhsa_exception_fp_denorm_src 0
		.amdhsa_exception_fp_ieee_div_zero 0
		.amdhsa_exception_fp_ieee_overflow 0
		.amdhsa_exception_fp_ieee_underflow 0
		.amdhsa_exception_fp_ieee_inexact 0
		.amdhsa_exception_int_div_zero 0
	.end_amdhsa_kernel

amdhsa.kernels:
  - .agpr_count:     0
    .args:
      - .offset:         0
        .size:           240
        .value_kind:     by_value
      - .actual_access:  write_only
        .address_space:  global
        .offset:         240
        .size:           8
        .value_kind:     global_buffer
      - .offset:         248
        .size:           4
        .value_kind:     hidden_block_count_x
      - .offset:         252
        .size:           4
        .value_kind:     hidden_block_count_y
      - .offset:         256
        .size:           4
        .value_kind:     hidden_block_count_z
      - .offset:         260
        .size:           2
        .value_kind:     hidden_group_size_x
      - .offset:         262
        .size:           2
        .value_kind:     hidden_group_size_y
      - .offset:         264
        .size:           2
        .value_kind:     hidden_group_size_z
      - .offset:         266
        .size:           2
        .value_kind:     hidden_remainder_x
      - .offset:         268
        .size:           2
        .value_kind:     hidden_remainder_y
      - .offset:         270
        .size:           2
        .value_kind:     hidden_remainder_z
      - .offset:         288
        .size:           8
        .value_kind:     hidden_global_offset_x
      - .offset:         296
        .size:           8
        .value_kind:     hidden_global_offset_y
      - .offset:         304
        .size:           8
        .value_kind:     hidden_global_offset_z
      - .offset:         312
        .size:           2
        .value_kind:     hidden_grid_dims
    .group_segment_fixed_size: 0
    .kernarg_segment_align: 8
    .kernarg_segment_size: 504
    .language:       OpenCL C
    .language_version:
      - 2
      - 0
    .max_flat_workgroup_size: 256
    .name:           _Z11prep_kernel8PrepArgsPc
    .private_segment_fixed_size: 0
    .sgpr_count:     50
    .sgpr_spill_count: 0
    .symbol:         _Z11prep_kernel8PrepArgsPc.kd
    .uniform_work_group_size: 1
    .uses_dynamic_stack: false
    .vgpr_count:     30
    .vgpr_spill_count: 0
    .wavefront_size: 64
  - .agpr_count:     16
    .args:
      - .actual_access:  read_only
        .address_space:  global
        .offset:         0
        .size:           8
        .value_kind:     global_buffer
      - .actual_access:  read_only
        .address_space:  global
        .offset:         8
        .size:           8
        .value_kind:     global_buffer
      - .actual_access:  read_only
        .address_space:  global
        .offset:         16
        .size:           8
        .value_kind:     global_buffer
      - .actual_access:  write_only
        .address_space:  global
        .offset:         24
        .size:           8
        .value_kind:     global_buffer
    .group_segment_fixed_size: 0
    .kernarg_segment_align: 8
    .kernarg_segment_size: 32
    .language:       OpenCL C
    .language_version:
      - 2
      - 0
    .max_flat_workgroup_size: 256
    .name:           _Z12conv1_kernelPKfPKDF16_S0_PDF16_
    .private_segment_fixed_size: 0
    .sgpr_count:     47
    .sgpr_spill_count: 0
    .symbol:         _Z12conv1_kernelPKfPKDF16_S0_PDF16_.kd
    .uniform_work_group_size: 1
    .uses_dynamic_stack: false
    .vgpr_count:     116
    .vgpr_spill_count: 0
    .wavefront_size: 64
  - .agpr_count:     32
    .args:
      - .actual_access:  read_only
        .address_space:  global
        .offset:         0
        .size:           8
        .value_kind:     global_buffer
      - .actual_access:  read_only
        .address_space:  global
        .offset:         8
        .size:           8
        .value_kind:     global_buffer
      - .actual_access:  read_only
        .address_space:  global
        .offset:         16
        .size:           8
        .value_kind:     global_buffer
      - .actual_access:  write_only
        .address_space:  global
        .offset:         24
        .size:           8
        .value_kind:     global_buffer
      - .actual_access:  write_only
        .address_space:  global
        .offset:         32
        .size:           8
        .value_kind:     global_buffer
    .group_segment_fixed_size: 0
    .kernarg_segment_align: 8
    .kernarg_segment_size: 40
    .language:       OpenCL C
    .language_version:
      - 2
      - 0
    .max_flat_workgroup_size: 64
    .name:           _Z11gat1_kernelPKDF16_S0_PKfPDF16_Pf
    .private_segment_fixed_size: 0
    .sgpr_count:     20
    .sgpr_spill_count: 0
    .symbol:         _Z11gat1_kernelPKDF16_S0_PKfPDF16_Pf.kd
    .uniform_work_group_size: 1
    .uses_dynamic_stack: false
    .vgpr_count:     284
    .vgpr_spill_count: 0
    .wavefront_size: 64
  - .agpr_count:     192
    .args:
      - .actual_access:  read_only
        .address_space:  global
        .offset:         0
        .size:           8
        .value_kind:     global_buffer
      - .actual_access:  read_only
        .address_space:  global
        .offset:         8
        .size:           8
        .value_kind:     global_buffer
      - .actual_access:  read_only
        .address_space:  global
        .offset:         16
        .size:           8
        .value_kind:     global_buffer
      - .actual_access:  read_only
        .address_space:  global
        .offset:         24
        .size:           8
        .value_kind:     global_buffer
      - .actual_access:  read_only
        .address_space:  global
        .offset:         32
        .size:           8
        .value_kind:     global_buffer
      - .actual_access:  write_only
        .address_space:  global
        .offset:         40
        .size:           8
        .value_kind:     global_buffer
      - .actual_access:  write_only
        .address_space:  global
        .offset:         48
        .size:           8
        .value_kind:     global_buffer
      - .actual_access:  read_only
        .address_space:  global
        .offset:         56
        .size:           8
        .value_kind:     global_buffer
      - .actual_access:  read_only
        .address_space:  global
        .offset:         64
        .size:           8
        .value_kind:     global_buffer
      - .actual_access:  read_only
        .address_space:  global
        .offset:         72
        .size:           8
        .value_kind:     global_buffer
      - .address_space:  global
        .offset:         80
        .size:           8
        .value_kind:     global_buffer
    .group_segment_fixed_size: 38016
    .kernarg_segment_align: 8
    .kernarg_segment_size: 88
    .language:       OpenCL C
    .language_version:
      - 2
      - 0
    .max_flat_workgroup_size: 256
    .name:           _Z11gat2_kernelPKfPKDF16_S0_S2_S0_PDF16_PfS2_S2_S0_S4_
    .private_segment_fixed_size: 0
    .sgpr_count:     22
    .sgpr_spill_count: 0
    .symbol:         _Z11gat2_kernelPKfPKDF16_S0_S2_S0_PDF16_PfS2_S2_S0_S4_.kd
    .uniform_work_group_size: 1
    .uses_dynamic_stack: false
    .vgpr_count:     424
    .vgpr_spill_count: 0
    .wavefront_size: 64
  - .agpr_count:     16
    .args:
      - .actual_access:  read_only
        .address_space:  global
        .offset:         0
        .size:           8
        .value_kind:     global_buffer
      - .actual_access:  read_only
        .address_space:  global
        .offset:         8
        .size:           8
        .value_kind:     global_buffer
      - .actual_access:  read_only
        .address_space:  global
        .offset:         16
        .size:           8
        .value_kind:     global_buffer
      - .address_space:  global
        .offset:         24
        .size:           8
        .value_kind:     global_buffer
    .group_segment_fixed_size: 1040
    .kernarg_segment_align: 8
    .kernarg_segment_size: 32
    .language:       OpenCL C
    .language_version:
      - 2
      - 0
    .max_flat_workgroup_size: 256
    .name:           _Z11gat3_kernelPKfPKDF16_S0_Pf
    .private_segment_fixed_size: 0
    .sgpr_count:     18
    .sgpr_spill_count: 0
    .symbol:         _Z11gat3_kernelPKfPKDF16_S0_Pf.kd
    .uniform_work_group_size: 1
    .uses_dynamic_stack: false
    .vgpr_count:     192
    .vgpr_spill_count: 0
    .wavefront_size: 64
  - .agpr_count:     0
    .args:
      - .actual_access:  read_only
        .address_space:  global
        .offset:         0
        .size:           8
        .value_kind:     global_buffer
      - .actual_access:  read_only
        .address_space:  global
        .offset:         8
        .size:           8
        .value_kind:     global_buffer
      - .actual_access:  read_only
        .address_space:  global
        .offset:         16
        .size:           8
        .value_kind:     global_buffer
      - .actual_access:  read_only
        .address_space:  global
        .offset:         24
        .size:           8
        .value_kind:     global_buffer
      - .actual_access:  read_only
        .address_space:  global
        .offset:         32
        .size:           8
        .value_kind:     global_buffer
      - .actual_access:  read_only
        .address_space:  global
        .offset:         40
        .size:           8
        .value_kind:     global_buffer
      - .actual_access:  write_only
        .address_space:  global
        .offset:         48
        .size:           8
        .value_kind:     global_buffer
    .group_segment_fixed_size: 87680
    .kernarg_segment_align: 8
    .kernarg_segment_size: 56
    .language:       OpenCL C
    .language_version:
      - 2
      - 0
    .max_flat_workgroup_size: 512
    .name:           _Z12gat3p_kernelPKfPKDF16_S0_S0_S0_S0_Pf
    .private_segment_fixed_size: 0
    .sgpr_count:     78
    .sgpr_spill_count: 0
    .symbol:         _Z12gat3p_kernelPKfPKDF16_S0_S0_S0_S0_Pf.kd
    .uniform_work_group_size: 1
    .uses_dynamic_stack: false
    .vgpr_count:     206
    .vgpr_spill_count: 0
    .wavefront_size: 64
  - .agpr_count:     0
    .args:
      - .actual_access:  read_only
        .address_space:  global
        .offset:         0
        .size:           8
        .value_kind:     global_buffer
      - .actual_access:  read_only
        .address_space:  global
        .offset:         8
        .size:           8
        .value_kind:     global_buffer
      - .actual_access:  read_only
        .address_space:  global
        .offset:         16
        .size:           8
        .value_kind:     global_buffer
      - .address_space:  global
        .offset:         24
        .size:           8
        .value_kind:     global_buffer
    .group_segment_fixed_size: 2048
    .kernarg_segment_align: 8
    .kernarg_segment_size: 32
    .language:       OpenCL C
    .language_version:
      - 2
      - 0
    .max_flat_workgroup_size: 64
    .name:           _Z12gat3s_kernelPKfPKDF16_S0_Pf
    .private_segment_fixed_size: 0
    .sgpr_count:     26
    .sgpr_spill_count: 0
    .symbol:         _Z12gat3s_kernelPKfPKDF16_S0_Pf.kd
    .uniform_work_group_size: 1
    .uses_dynamic_stack: false
    .vgpr_count:     192
    .vgpr_spill_count: 0
    .wavefront_size: 64
  - .agpr_count:     0
    .args:
      - .actual_access:  read_only
        .address_space:  global
        .offset:         0
        .size:           8
        .value_kind:     global_buffer
      - .actual_access:  read_only
        .address_space:  global
        .offset:         8
        .size:           8
        .value_kind:     global_buffer
      - .actual_access:  read_only
        .address_space:  global
        .offset:         16
        .size:           8
        .value_kind:     global_buffer
      - .actual_access:  write_only
        .address_space:  global
        .offset:         24
        .size:           8
        .value_kind:     global_buffer
    .group_segment_fixed_size: 13952
    .kernarg_segment_align: 8
    .kernarg_segment_size: 32
    .language:       OpenCL C
    .language_version:
      - 2
      - 0
    .max_flat_workgroup_size: 256
    .name:           _Z11head_kernelPKfS0_S0_Pf
    .private_segment_fixed_size: 0
    .sgpr_count:     15
    .sgpr_spill_count: 0
    .symbol:         _Z11head_kernelPKfS0_S0_Pf.kd
    .uniform_work_group_size: 1
    .uses_dynamic_stack: false
    .vgpr_count:     38
    .vgpr_spill_count: 0
    .wavefront_size: 64
  - .agpr_count:     0
    .args:
      - .actual_access:  read_only
        .address_space:  global
        .offset:         0
        .size:           8
        .value_kind:     global_buffer
      - .actual_access:  read_only
        .address_space:  global
        .offset:         8
        .size:           8
        .value_kind:     global_buffer
      - .actual_access:  read_only
        .address_space:  global
        .offset:         16
        .size:           8
        .value_kind:     global_buffer
      - .actual_access:  write_only
        .address_space:  global
        .offset:         24
        .size:           8
        .value_kind:     global_buffer
    .group_segment_fixed_size: 640
    .kernarg_segment_align: 8
    .kernarg_segment_size: 32
    .language:       OpenCL C
    .language_version:
      - 2
      - 0
    .max_flat_workgroup_size: 256
    .name:           _Z12final_kernelPKfS0_S0_Pf
    .private_segment_fixed_size: 0
    .sgpr_count:     18
    .sgpr_spill_count: 0
    .symbol:         _Z12final_kernelPKfS0_S0_Pf.kd
    .uniform_work_group_size: 1
    .uses_dynamic_stack: false
    .vgpr_count:     37
    .vgpr_spill_count: 0
    .wavefront_size: 64
  - .agpr_count:     0
    .args:
      - .actual_access:  read_only
        .address_space:  global
        .offset:         0
        .size:           8
        .value_kind:     global_buffer
      - .address_space:  global
        .offset:         8
        .size:           8
        .value_kind:     global_buffer
      - .actual_access:  read_only
        .address_space:  global
        .offset:         16
        .size:           8
        .value_kind:     global_buffer
      - .actual_access:  write_only
        .address_space:  global
        .offset:         24
        .size:           8
        .value_kind:     global_buffer
      - .actual_access:  read_only
        .address_space:  global
        .offset:         32
        .size:           8
        .value_kind:     global_buffer
      - .actual_access:  read_only
        .address_space:  global
        .offset:         40
        .size:           8
        .value_kind:     global_buffer
      - .actual_access:  read_only
        .address_space:  global
        .offset:         48
        .size:           8
        .value_kind:     global_buffer
      - .actual_access:  read_only
        .address_space:  global
        .offset:         56
        .size:           8
        .value_kind:     global_buffer
      - .offset:         64
        .size:           4
        .value_kind:     hidden_block_count_x
      - .offset:         68
        .size:           4
        .value_kind:     hidden_block_count_y
      - .offset:         72
        .size:           4
        .value_kind:     hidden_block_count_z
      - .offset:         76
        .size:           2
        .value_kind:     hidden_group_size_x
      - .offset:         78
        .size:           2
        .value_kind:     hidden_group_size_y
      - .offset:         80
        .size:           2
        .value_kind:     hidden_group_size_z
      - .offset:         82
        .size:           2
        .value_kind:     hidden_remainder_x
      - .offset:         84
        .size:           2
        .value_kind:     hidden_remainder_y
      - .offset:         86
        .size:           2
        .value_kind:     hidden_remainder_z
      - .offset:         104
        .size:           8
        .value_kind:     hidden_global_offset_x
      - .offset:         112
        .size:           8
        .value_kind:     hidden_global_offset_y
      - .offset:         120
        .size:           8
        .value_kind:     hidden_global_offset_z
      - .offset:         128
        .size:           2
        .value_kind:     hidden_grid_dims
    .group_segment_fixed_size: 74240
    .kernarg_segment_align: 8
    .kernarg_segment_size: 320
    .language:       OpenCL C
    .language_version:
      - 2
      - 0
    .max_flat_workgroup_size: 256
    .name:           _Z11conv_kernelILi64ELi128ELi128ELi128ELi4ELi2ELi2ELb1ELi1ELb0ELb0ELi2EEvPKDF16_S1_PKfPDF16_S1_S3_S1_S3_
    .private_segment_fixed_size: 0
    .sgpr_count:     58
    .sgpr_spill_count: 0
    .symbol:         _Z11conv_kernelILi64ELi128ELi128ELi128ELi4ELi2ELi2ELb1ELi1ELb0ELb0ELi2EEvPKDF16_S1_PKfPDF16_S1_S3_S1_S3_.kd
    .uniform_work_group_size: 1
    .uses_dynamic_stack: false
    .vgpr_count:     256
    .vgpr_spill_count: 0
    .wavefront_size: 64
  - .agpr_count:     0
    .args:
      - .address_space:  global
        .offset:         0
        .size:           8
        .value_kind:     global_buffer
      - .address_space:  global
        .offset:         8
        .size:           8
        .value_kind:     global_buffer
      - .actual_access:  read_only
        .address_space:  global
        .offset:         16
        .size:           8
        .value_kind:     global_buffer
      - .actual_access:  write_only
        .address_space:  global
        .offset:         24
        .size:           8
        .value_kind:     global_buffer
      - .address_space:  global
        .offset:         32
        .size:           8
        .value_kind:     global_buffer
      - .actual_access:  read_only
        .address_space:  global
        .offset:         40
        .size:           8
        .value_kind:     global_buffer
      - .actual_access:  read_only
        .address_space:  global
        .offset:         48
        .size:           8
        .value_kind:     global_buffer
      - .actual_access:  read_only
        .address_space:  global
        .offset:         56
        .size:           8
        .value_kind:     global_buffer
      - .offset:         64
        .size:           4
        .value_kind:     hidden_block_count_x
      - .offset:         68
        .size:           4
        .value_kind:     hidden_block_count_y
      - .offset:         72
        .size:           4
        .value_kind:     hidden_block_count_z
      - .offset:         76
        .size:           2
        .value_kind:     hidden_group_size_x
      - .offset:         78
        .size:           2
        .value_kind:     hidden_group_size_y
      - .offset:         80
        .size:           2
        .value_kind:     hidden_group_size_z
      - .offset:         82
        .size:           2
        .value_kind:     hidden_remainder_x
      - .offset:         84
        .size:           2
        .value_kind:     hidden_remainder_y
      - .offset:         86
        .size:           2
        .value_kind:     hidden_remainder_z
      - .offset:         104
        .size:           8
        .value_kind:     hidden_global_offset_x
      - .offset:         112
        .size:           8
        .value_kind:     hidden_global_offset_y
      - .offset:         120
        .size:           8
        .value_kind:     hidden_global_offset_z
      - .offset:         128
        .size:           2
        .value_kind:     hidden_grid_dims
    .group_segment_fixed_size: 148480
    .kernarg_segment_align: 8
    .kernarg_segment_size: 320
    .language:       OpenCL C
    .language_version:
      - 2
      - 0
    .max_flat_workgroup_size: 512
    .name:           _Z11conv_kernelILi128ELi256ELi64ELi64ELi4ELi2ELi4ELb0ELi1ELb1ELb0ELi1EEvPKDF16_S1_PKfPDF16_S1_S3_S1_S3_
    .private_segment_fixed_size: 0
    .sgpr_count:     28
    .sgpr_spill_count: 0
    .symbol:         _Z11conv_kernelILi128ELi256ELi64ELi64ELi4ELi2ELi4ELb0ELi1ELb1ELb0ELi1EEvPKDF16_S1_PKfPDF16_S1_S3_S1_S3_.kd
    .uniform_work_group_size: 1
    .uses_dynamic_stack: false
    .vgpr_count:     234
    .vgpr_spill_count: 0
    .wavefront_size: 64
  - .agpr_count:     0
    .args:
      - .address_space:  global
        .offset:         0
        .size:           8
        .value_kind:     global_buffer
      - .address_space:  global
        .offset:         8
        .size:           8
        .value_kind:     global_buffer
      - .actual_access:  read_only
        .address_space:  global
        .offset:         16
        .size:           8
        .value_kind:     global_buffer
      - .actual_access:  write_only
        .address_space:  global
        .offset:         24
        .size:           8
        .value_kind:     global_buffer
      - .address_space:  global
        .offset:         32
        .size:           8
        .value_kind:     global_buffer
      - .actual_access:  read_only
        .address_space:  global
        .offset:         40
        .size:           8
        .value_kind:     global_buffer
      - .actual_access:  read_only
        .address_space:  global
        .offset:         48
        .size:           8
        .value_kind:     global_buffer
      - .actual_access:  read_only
        .address_space:  global
        .offset:         56
        .size:           8
        .value_kind:     global_buffer
      - .offset:         64
        .size:           4
        .value_kind:     hidden_block_count_x
      - .offset:         68
        .size:           4
        .value_kind:     hidden_block_count_y
      - .offset:         72
        .size:           4
        .value_kind:     hidden_block_count_z
      - .offset:         76
        .size:           2
        .value_kind:     hidden_group_size_x
      - .offset:         78
        .size:           2
        .value_kind:     hidden_group_size_y
      - .offset:         80
        .size:           2
        .value_kind:     hidden_group_size_z
      - .offset:         82
        .size:           2
        .value_kind:     hidden_remainder_x
      - .offset:         84
        .size:           2
        .value_kind:     hidden_remainder_y
      - .offset:         86
        .size:           2
        .value_kind:     hidden_remainder_z
      - .offset:         104
        .size:           8
        .value_kind:     hidden_global_offset_x
      - .offset:         112
        .size:           8
        .value_kind:     hidden_global_offset_y
      - .offset:         120
        .size:           8
        .value_kind:     hidden_global_offset_z
      - .offset:         128
        .size:           2
        .value_kind:     hidden_grid_dims
    .group_segment_fixed_size: 157696
    .kernarg_segment_align: 8
    .kernarg_segment_size: 320
    .language:       OpenCL C
    .language_version:
      - 2
      - 0
    .max_flat_workgroup_size: 512
    .name:           _Z11conv_kernelILi256ELi256ELi32ELi32ELi2ELi2ELi2ELb0ELi2ELb0ELb1ELi1EEvPKDF16_S1_PKfPDF16_S1_S3_S1_S3_
    .private_segment_fixed_size: 0
    .sgpr_count:     30
    .sgpr_spill_count: 0
    .symbol:         _Z11conv_kernelILi256ELi256ELi32ELi32ELi2ELi2ELi2ELb0ELi2ELb0ELb1ELi1EEvPKDF16_S1_PKfPDF16_S1_S3_S1_S3_.kd
    .uniform_work_group_size: 1
    .uses_dynamic_stack: false
    .vgpr_count:     121
    .vgpr_spill_count: 0
    .wavefront_size: 64
